# MLA online softmax: running max only advanced when the tile max exceeds it by more than 8 (log2 units), so the accumulator rescale is skipped on almost all tiles (exact identity, f32 state)
# speedup vs baseline: 1.0079x; 1.0079x over previous
; template <bool MLA>
; __device__ __forceinline__ void attn_unit(const P& p, LAS unsigned char* lds, const int b, const int h, const int qb) {
;     ...
;                 float pm = -3.0e38f;
;                 if (k0 + 63 > qw) {
; #pragma unroll
;                     for (int r = 0; r < 16; ++r) { const int c = (r & 3) + 8 * (r >> 2);
;                         if (c > dq) p0[r] = -__builtin_inff(); if (c + 32 > dq) p1[r] = -__builtin_inff(); }
;                 }
; #pragma unroll
;                 for (int r = 0; r < 16; ++r) pm = fmaxf(pm, fmaxf(p0[r], p1[r]));
;                 pm = fmaxf(pm, __shfl_xor(pm, 32));
;                 const float mn = fmaxf(m_run, pm), alpha = __builtin_amdgcn_exp2f(m_run - mn); m_run = mn;
;                 float ps = 0.f;
; #pragma unroll
;                 for (int r = 0; r < 16; ++r) { p0[r] = __builtin_amdgcn_exp2f(p0[r] - mn); p1[r] = __builtin_amdgcn_exp2f(p1[r] - mn); ps += p0[r] + p1[r]; }
;                 ps += __shfl_xor(ps, 32);
;                 l_run = l_run * alpha + ps;
;                 if (__any(alpha < 1.f)) { if (hi == 0) al[r32] = alpha; asm volatile("s_waitcnt lgkmcnt(0)" ::: "memory");
; #pragma unroll
;                     for (int r = 0; r < 16; ++r) { const float a = al[(r & 3) + 8 * (r >> 2) + 4 * hi];
; #pragma unroll
;                         for (int d0 = 0; d0 < 4; ++d0) o[d0][r] *= a; } }
.LBB0_711:
	s_nop 8
	s_mov_b32 s0, 0xff61b1e6
	v_max3_f32 v3, v82, v83, s0
	v_max3_f32 v4, v84, v85, v86
	v_max3_f32 v5, v87, v88, v89
	v_max3_f32 v3, v3, v90, v91
	v_max3_f32 v4, v4, v92, v93
	v_max3_f32 v5, v5, v94, v95
	v_max3_f32 v3, v3, v96, v97
	v_max3_f32 v4, v4, v98, v99
	v_max3_f32 v5, v5, v100, v101
	v_max3_f32 v3, v3, v102, v103
	v_max3_f32 v4, v4, v104, v105
	v_max3_f32 v5, v5, v106, v107
	v_max3_f32 v3, v3, v108, v109
	v_max3_f32 v4, v4, v110, v111
	v_max3_f32 v5, v5, v112, v113
	v_max3_f32 v3, v3, v4, v5
	v_and_b32_e32 v5, 64, v211
	v_xor_b32_e32 v4, 32, v211
	v_add_u32_e32 v5, 64, v5
	v_cmp_lt_i32_e32 vcc, v4, v5
	s_nop 1
	v_cndmask_b32_e32 v4, v211, v4, vcc
	v_lshlrev_b32_e32 v217, 2, v4
	ds_bpermute_b32 v4, v217, v3
	s_waitcnt lgkmcnt(0)
	v_max_f32_e32 v3, v3, v4
	v_add_f32_e32 v4, 0xc1000000, v3
	v_cmp_gt_f32_e32 vcc, v4, v216
	s_nop 1
	v_cndmask_b32_e32 v3, v216, v3, vcc
	v_sub_f32_e32 v4, v82, v3
	v_exp_f32_e32 v10, v4
	v_sub_f32_e32 v4, v98, v3
	v_exp_f32_e32 v4, v4
	v_sub_f32_e32 v5, v83, v3
	v_exp_f32_e32 v12, v5
	v_sub_f32_e32 v5, v99, v3
	v_add_f32_e32 v6, v10, v4
	v_add_f32_e32 v8, 0, v6
	v_sub_f32_e32 v6, v84, v3
	v_exp_f32_e32 v5, v5
	v_exp_f32_e32 v14, v6
	v_sub_f32_e32 v6, v100, v3
	v_exp_f32_e32 v6, v6
	v_add_f32_e32 v9, v12, v5
	v_sub_f32_e32 v7, v85, v3
	v_add_f32_e32 v8, v9, v8
	v_add_f32_e32 v9, v14, v6
	v_exp_f32_e32 v16, v7
	v_sub_f32_e32 v7, v101, v3
	v_add_f32_e32 v11, v9, v8
	v_sub_f32_e32 v8, v86, v3
	v_exp_f32_e32 v7, v7
	v_exp_f32_e32 v84, v8
	v_sub_f32_e32 v8, v102, v3
	v_exp_f32_e32 v8, v8
	v_add_f32_e32 v13, v16, v7
	v_sub_f32_e32 v9, v87, v3
	v_add_f32_e32 v11, v13, v11
	v_add_f32_e32 v13, v84, v8
	v_exp_f32_e32 v87, v9
	v_sub_f32_e32 v9, v103, v3
	v_add_f32_e32 v15, v13, v11
	v_sub_f32_e32 v11, v88, v3
	v_exp_f32_e32 v9, v9
	v_exp_f32_e32 v98, v11
	v_sub_f32_e32 v11, v104, v3
	v_exp_f32_e32 v11, v11
	v_add_f32_e32 v17, v87, v9
	v_sub_f32_e32 v13, v89, v3
	v_add_f32_e32 v15, v17, v15
	v_add_f32_e32 v17, v98, v11
	v_exp_f32_e32 v99, v13
	v_sub_f32_e32 v13, v105, v3
	v_add_f32_e32 v82, v17, v15
	v_sub_f32_e32 v15, v90, v3
	v_exp_f32_e32 v13, v13
	v_exp_f32_e32 v83, v15
	v_sub_f32_e32 v15, v106, v3
	v_exp_f32_e32 v15, v15
	v_add_f32_e32 v85, v99, v13
	v_sub_f32_e32 v17, v91, v3
	v_add_f32_e32 v82, v85, v82
	v_add_f32_e32 v85, v83, v15
	v_exp_f32_e32 v86, v17
	v_sub_f32_e32 v17, v107, v3
	v_add_f32_e32 v89, v85, v82
	v_sub_f32_e32 v82, v92, v3
	v_exp_f32_e32 v17, v17
	v_exp_f32_e32 v88, v82
	v_sub_f32_e32 v82, v108, v3
	v_exp_f32_e32 v82, v82
	v_add_f32_e32 v91, v86, v17
	v_sub_f32_e32 v85, v93, v3
	v_add_f32_e32 v89, v91, v89
	v_add_f32_e32 v91, v88, v82
	v_exp_f32_e32 v90, v85
	v_sub_f32_e32 v85, v109, v3
	v_add_f32_e32 v93, v91, v89
	v_sub_f32_e32 v89, v94, v3
	v_exp_f32_e32 v85, v85
	v_exp_f32_e32 v92, v89
	v_sub_f32_e32 v89, v110, v3
	v_exp_f32_e32 v89, v89
	v_add_f32_e32 v100, v90, v85
	v_sub_f32_e32 v91, v95, v3
	v_add_f32_e32 v93, v100, v93
	v_add_f32_e32 v95, v92, v89
	v_exp_f32_e32 v94, v91
	v_sub_f32_e32 v91, v111, v3
	v_add_f32_e32 v100, v95, v93
	v_sub_f32_e32 v93, v96, v3
	v_exp_f32_e32 v91, v91
	v_exp_f32_e32 v101, v93
	v_sub_f32_e32 v93, v112, v3
	v_sub_f32_e32 v95, v97, v3
	v_exp_f32_e32 v93, v93
	v_exp_f32_e32 v102, v95
	v_sub_f32_e32 v95, v113, v3
	v_exp_f32_e32 v95, v95
	v_add_f32_e32 v103, v94, v91
	v_add_f32_e32 v96, v103, v100
	v_add_f32_e32 v97, v101, v93
	v_add_f32_e32 v97, v97, v96
	v_add_f32_e32 v100, v102, v95
	v_sub_f32_e32 v216, v216, v3
	v_add_f32_e32 v97, v100, v97
	v_exp_f32_e32 v96, v216
	ds_bpermute_b32 v100, v217, v97
	v_cmp_gt_f32_e32 vcc, 1.0, v96
	s_cbranch_vccz .LBB0_715
	s_and_saveexec_b64 s[0:1], s[4:5]
	ds_write_b32 v212, v96
	s_or_b64 exec, exec, s[0:1]
	s_waitcnt lgkmcnt(0)
	ds_read_b128 v[104:107], v214 offset:96
	ds_read_b128 v[108:111], v214 offset:64
	ds_read_b128 v[216:219], v214 offset:32
	ds_read_b128 v[220:223], v214
	s_waitcnt lgkmcnt(3)
	v_pk_mul_f32 v[80:81], v[80:81], v[106:107]
	s_waitcnt lgkmcnt(2)
	v_pk_mul_f32 v[76:77], v[76:77], v[110:111]
	s_waitcnt lgkmcnt(1)
	v_pk_mul_f32 v[72:73], v[72:73], v[218:219]
	s_waitcnt lgkmcnt(0)
	v_pk_mul_f32 v[68:69], v[68:69], v[222:223]
	v_pk_mul_f32 v[78:79], v[78:79], v[104:105]
	v_pk_mul_f32 v[74:75], v[74:75], v[108:109]
	v_pk_mul_f32 v[70:71], v[70:71], v[216:217]
	v_pk_mul_f32 v[66:67], v[66:67], v[220:221]
	v_pk_mul_f32 v[64:65], v[64:65], v[106:107]
	v_pk_mul_f32 v[60:61], v[60:61], v[110:111]
	v_pk_mul_f32 v[56:57], v[56:57], v[218:219]
	v_pk_mul_f32 v[52:53], v[52:53], v[222:223]
	v_pk_mul_f32 v[62:63], v[62:63], v[104:105]
	v_pk_mul_f32 v[58:59], v[58:59], v[108:109]
	v_pk_mul_f32 v[54:55], v[54:55], v[216:217]
	v_pk_mul_f32 v[50:51], v[50:51], v[220:221]
	v_pk_mul_f32 v[48:49], v[48:49], v[106:107]
	v_pk_mul_f32 v[44:45], v[44:45], v[110:111]
	v_pk_mul_f32 v[40:41], v[40:41], v[218:219]
	v_pk_mul_f32 v[36:37], v[36:37], v[222:223]
	v_pk_mul_f32 v[46:47], v[46:47], v[104:105]
	v_pk_mul_f32 v[42:43], v[42:43], v[108:109]
	v_pk_mul_f32 v[38:39], v[38:39], v[216:217]
	v_pk_mul_f32 v[34:35], v[34:35], v[220:221]
	v_pk_mul_f32 v[32:33], v[32:33], v[106:107]
	v_pk_mul_f32 v[28:29], v[28:29], v[110:111]
	v_pk_mul_f32 v[24:25], v[24:25], v[218:219]
	v_pk_mul_f32 v[20:21], v[20:21], v[222:223]
	v_pk_mul_f32 v[30:31], v[30:31], v[104:105]
	v_pk_mul_f32 v[26:27], v[26:27], v[108:109]
	v_pk_mul_f32 v[22:23], v[22:23], v[216:217]
	v_pk_mul_f32 v[18:19], v[18:19], v[220:221]

; template <bool MLA>
; __device__ __forceinline__ void attn_unit(const P& p, LAS unsigned char* lds, const int b, const int h, const int qb) {
;     ...
;                 float pm = -3.0e38f;
;                 if (k0 + 63 > qw) {
; #pragma unroll
;                     for (int r = 0; r < 16; ++r) { const int c = (r & 3) + 8 * (r >> 2);
;                         if (c > dq) p0[r] = -__builtin_inff(); if (c + 32 > dq) p1[r] = -__builtin_inff(); }
;                 }
; #pragma unroll
;                 for (int r = 0; r < 16; ++r) pm = fmaxf(pm, fmaxf(p0[r], p1[r]));
;                 pm = fmaxf(pm, __shfl_xor(pm, 32));
;                 const float mn = fmaxf(m_run, pm), alpha = __builtin_amdgcn_exp2f(m_run - mn); m_run = mn;
;                 float ps = 0.f;
; #pragma unroll
;                 for (int r = 0; r < 16; ++r) { p0[r] = __builtin_amdgcn_exp2f(p0[r] - mn); p1[r] = __builtin_amdgcn_exp2f(p1[r] - mn); ps += p0[r] + p1[r]; }
;                 ps += __shfl_xor(ps, 32);
;                 l_run = l_run * alpha + ps;
;                 if (__any(alpha < 1.f)) { if (hi == 0) al[r32] = alpha; asm volatile("s_waitcnt lgkmcnt(0)" ::: "memory");
; #pragma unroll
;                     for (int r = 0; r < 16; ++r) { const float a = al[(r & 3) + 8 * (r >> 2) + 4 * hi];
; #pragma unroll
;                         for (int d0 = 0; d0 < 4; ++d0) o[d0][r] *= a; } }
.LBB0_877:
	s_nop 8
	s_mov_b32 s0, 0xff61b1e6
	v_max3_f32 v3, v82, v83, s0
	v_max3_f32 v4, v84, v85, v86
	v_max3_f32 v5, v87, v88, v89
	v_max3_f32 v3, v3, v90, v91
	v_max3_f32 v4, v4, v92, v93
	v_max3_f32 v5, v5, v94, v95
	v_max3_f32 v3, v3, v96, v97
	v_max3_f32 v4, v4, v98, v99
	v_max3_f32 v5, v5, v100, v101
	v_max3_f32 v3, v3, v102, v103
	v_max3_f32 v4, v4, v104, v105
	v_max3_f32 v5, v5, v106, v107
	v_max3_f32 v3, v3, v108, v109
	v_max3_f32 v4, v4, v110, v111
	v_max3_f32 v5, v5, v112, v113
	v_max3_f32 v3, v3, v4, v5
	v_and_b32_e32 v5, 64, v214
	v_xor_b32_e32 v4, 32, v214
	v_add_u32_e32 v5, 64, v5
	v_cmp_lt_i32_e32 vcc, v4, v5
	s_nop 1
	v_cndmask_b32_e32 v4, v214, v4, vcc
	v_lshlrev_b32_e32 v220, 2, v4
	ds_bpermute_b32 v4, v220, v3
	s_waitcnt lgkmcnt(0)
	v_max_f32_e32 v3, v3, v4
	v_add_f32_e32 v4, 0xc1000000, v3
	v_cmp_gt_f32_e32 vcc, v4, v219
	s_nop 1
	v_cndmask_b32_e32 v3, v219, v3, vcc
	v_sub_f32_e32 v4, v82, v3
	v_exp_f32_e32 v10, v4
	v_sub_f32_e32 v4, v98, v3
	v_exp_f32_e32 v4, v4
	v_sub_f32_e32 v5, v83, v3
	v_exp_f32_e32 v12, v5
	v_sub_f32_e32 v5, v99, v3
	v_add_f32_e32 v6, v10, v4
	v_add_f32_e32 v8, 0, v6
	v_sub_f32_e32 v6, v84, v3
	v_exp_f32_e32 v5, v5
	v_exp_f32_e32 v14, v6
	v_sub_f32_e32 v6, v100, v3
	v_exp_f32_e32 v6, v6
	v_add_f32_e32 v9, v12, v5
	v_sub_f32_e32 v7, v85, v3
	v_add_f32_e32 v8, v9, v8
	v_add_f32_e32 v9, v14, v6
	v_exp_f32_e32 v16, v7
	v_sub_f32_e32 v7, v101, v3
	v_add_f32_e32 v11, v9, v8
	v_sub_f32_e32 v8, v86, v3
	v_exp_f32_e32 v7, v7
	v_exp_f32_e32 v84, v8
	v_sub_f32_e32 v8, v102, v3
	v_exp_f32_e32 v8, v8
	v_add_f32_e32 v13, v16, v7
	v_sub_f32_e32 v9, v87, v3
	v_add_f32_e32 v11, v13, v11
	v_add_f32_e32 v13, v84, v8
	v_exp_f32_e32 v87, v9
	v_sub_f32_e32 v9, v103, v3
	v_add_f32_e32 v15, v13, v11
	v_sub_f32_e32 v11, v88, v3
	v_exp_f32_e32 v9, v9
	v_exp_f32_e32 v98, v11
	v_sub_f32_e32 v11, v104, v3
	v_exp_f32_e32 v11, v11
	v_add_f32_e32 v17, v87, v9
	v_sub_f32_e32 v13, v89, v3
	v_add_f32_e32 v15, v17, v15
	v_add_f32_e32 v17, v98, v11
	v_exp_f32_e32 v99, v13
	v_sub_f32_e32 v13, v105, v3
	v_add_f32_e32 v82, v17, v15
	v_sub_f32_e32 v15, v90, v3
	v_exp_f32_e32 v13, v13
	v_exp_f32_e32 v83, v15
	v_sub_f32_e32 v15, v106, v3
	v_exp_f32_e32 v15, v15
	v_add_f32_e32 v85, v99, v13
	v_sub_f32_e32 v17, v91, v3
	v_add_f32_e32 v82, v85, v82
	v_add_f32_e32 v85, v83, v15
	v_exp_f32_e32 v86, v17
	v_sub_f32_e32 v17, v107, v3
	v_add_f32_e32 v89, v85, v82
	v_sub_f32_e32 v82, v92, v3
	v_exp_f32_e32 v17, v17
	v_exp_f32_e32 v88, v82
	v_sub_f32_e32 v82, v108, v3
	v_exp_f32_e32 v82, v82
	v_add_f32_e32 v91, v86, v17
	v_sub_f32_e32 v85, v93, v3
	v_add_f32_e32 v89, v91, v89
	v_add_f32_e32 v91, v88, v82
	v_exp_f32_e32 v90, v85
	v_sub_f32_e32 v85, v109, v3
	v_add_f32_e32 v93, v91, v89
	v_sub_f32_e32 v89, v94, v3
	v_exp_f32_e32 v85, v85
	v_exp_f32_e32 v92, v89
	v_sub_f32_e32 v89, v110, v3
	v_exp_f32_e32 v89, v89
	v_add_f32_e32 v100, v90, v85
	v_sub_f32_e32 v91, v95, v3
	v_add_f32_e32 v93, v100, v93
	v_add_f32_e32 v95, v92, v89
	v_exp_f32_e32 v94, v91
	v_sub_f32_e32 v91, v111, v3
	v_add_f32_e32 v100, v95, v93
	v_sub_f32_e32 v93, v96, v3
	v_exp_f32_e32 v91, v91
	v_exp_f32_e32 v101, v93
	v_sub_f32_e32 v93, v112, v3
	v_sub_f32_e32 v95, v97, v3
	v_exp_f32_e32 v93, v93
	v_exp_f32_e32 v102, v95
	v_sub_f32_e32 v95, v113, v3
	v_exp_f32_e32 v95, v95
	v_add_f32_e32 v103, v94, v91
	v_add_f32_e32 v96, v103, v100
	v_add_f32_e32 v97, v101, v93
	v_add_f32_e32 v97, v97, v96
	v_add_f32_e32 v100, v102, v95
	v_sub_f32_e32 v219, v219, v3
	v_add_f32_e32 v97, v100, v97
	v_exp_f32_e32 v96, v219
	ds_bpermute_b32 v100, v220, v97
	v_cmp_gt_f32_e32 vcc, 1.0, v96
	s_cbranch_vccz .LBB0_881
	s_and_saveexec_b64 s[0:1], s[4:5]
	ds_write_b32 v215, v96
	s_or_b64 exec, exec, s[0:1]
	s_waitcnt lgkmcnt(0)
	ds_read_b128 v[104:107], v217 offset:96
	ds_read_b128 v[108:111], v217 offset:64
	ds_read_b128 v[220:223], v217 offset:32
	ds_read_b128 v[224:227], v217
	s_waitcnt lgkmcnt(3)
	v_pk_mul_f32 v[80:81], v[80:81], v[106:107]
	s_waitcnt lgkmcnt(2)
	v_pk_mul_f32 v[76:77], v[76:77], v[110:111]
	s_waitcnt lgkmcnt(1)
	v_pk_mul_f32 v[72:73], v[72:73], v[222:223]
	s_waitcnt lgkmcnt(0)
	v_pk_mul_f32 v[68:69], v[68:69], v[226:227]
	v_pk_mul_f32 v[78:79], v[78:79], v[104:105]
	v_pk_mul_f32 v[74:75], v[74:75], v[108:109]
	v_pk_mul_f32 v[70:71], v[70:71], v[220:221]
	v_pk_mul_f32 v[66:67], v[66:67], v[224:225]
	v_pk_mul_f32 v[64:65], v[64:65], v[106:107]
	v_pk_mul_f32 v[60:61], v[60:61], v[110:111]
	v_pk_mul_f32 v[56:57], v[56:57], v[222:223]
	v_pk_mul_f32 v[52:53], v[52:53], v[226:227]
	v_pk_mul_f32 v[62:63], v[62:63], v[104:105]
	v_pk_mul_f32 v[58:59], v[58:59], v[108:109]
	v_pk_mul_f32 v[54:55], v[54:55], v[220:221]
	v_pk_mul_f32 v[50:51], v[50:51], v[224:225]
	v_pk_mul_f32 v[48:49], v[48:49], v[106:107]
	v_pk_mul_f32 v[44:45], v[44:45], v[110:111]
	v_pk_mul_f32 v[40:41], v[40:41], v[222:223]
	v_pk_mul_f32 v[36:37], v[36:37], v[226:227]
	v_pk_mul_f32 v[46:47], v[46:47], v[104:105]
	v_pk_mul_f32 v[42:43], v[42:43], v[108:109]
	v_pk_mul_f32 v[38:39], v[38:39], v[220:221]
	v_pk_mul_f32 v[34:35], v[34:35], v[224:225]
	v_pk_mul_f32 v[32:33], v[32:33], v[106:107]
	v_pk_mul_f32 v[28:29], v[28:29], v[110:111]
	v_pk_mul_f32 v[24:25], v[24:25], v[222:223]
	v_pk_mul_f32 v[20:21], v[20:21], v[226:227]
	v_pk_mul_f32 v[30:31], v[30:31], v[104:105]
	v_pk_mul_f32 v[26:27], v[26:27], v[108:109]
	v_pk_mul_f32 v[22:23], v[22:23], v[220:221]
	v_pk_mul_f32 v[18:19], v[18:19], v[224:225]
